# speedup vs baseline: 1.0079x; 1.0079x over previous
.LBB0_63:
	s_or_b64 exec, exec, s[2:3]
	v_lshrrev_b32_e32 v6, 2, v1
	v_lshrrev_b32_e32 v5, 4, v1
	v_and_b32_e32 v6, 8, v6
	s_mov_b32 s0, 0x1fffff0
	v_and_b32_e32 v4, 31, v1
	v_and_or_b32 v5, v5, s0, v6
	v_lshrrev_b32_e32 v1, 1, v1
	s_movk_i32 s0, 0x60
	v_and_or_b32 v1, v1, s0, v4
	v_lshl_or_b32 v4, v5, 7, v1
	v_ashrrev_i32_e32 v5, 31, v4
	v_lshl_add_u64 v[2:3], v[4:5], 2, v[2:3]
	global_load_dword v6, v[2:3], off offset:1024
	global_load_dword v7, v[2:3], off offset:1536
	global_load_dword v4, v[2:3], off offset:2048
	global_load_dword v5, v[2:3], off offset:3072
	global_load_dword v8, v[2:3], off offset:3584
	global_load_dword v9, v[2:3], off offset:2560
	global_load_dword v10, v[2:3], off
	global_load_dword v11, v[2:3], off offset:512
	v_ashrrev_i32_e32 v1, 31, v0
	v_lshl_add_u64 v[0:1], v[0:1], 4, s[4:5]
	s_waitcnt vmcnt(6)
	v_cvt_pk_f16_f32 v3, v6, v7
	s_waitcnt vmcnt(3)
	v_cvt_pk_f16_f32 v5, v5, v8
	s_waitcnt vmcnt(2)
	v_cvt_pk_f16_f32 v4, v4, v9
	s_waitcnt vmcnt(0)
	v_cvt_pk_f16_f32 v2, v10, v11
	global_store_dwordx4 v[0:1], v[2:5], off sc1
	s_endpgm
	s_nop 0
	s_nop 0
	s_nop 0
	s_nop 0
	s_nop 0
	s_nop 0
	s_nop 0
	s_nop 0
	s_nop 0
	s_nop 0
	s_nop 0
	s_nop 0
	s_nop 0
	s_nop 0
	s_nop 0
	s_nop 0
	s_nop 0
	s_nop 0
	s_nop 0
	s_nop 0
	s_nop 0
	s_nop 0
	s_nop 0
	s_nop 0
	s_nop 0
	s_nop 0
	s_nop 0
	s_nop 0
	s_nop 0
	s_nop 0
	s_nop 0
	s_nop 0
	s_nop 0
	s_nop 0
	s_nop 0
	s_nop 0
	s_nop 0
	s_nop 0
	s_nop 0
	s_nop 0
	s_nop 0
	s_nop 0
	s_nop 0
	s_nop 0
	s_nop 0
	s_nop 0
	s_nop 0
	s_nop 0
	s_nop 0
	s_nop 0
	s_nop 0
	s_nop 0
	s_nop 0
	s_nop 0
	s_nop 0
	s_nop 0
	s_nop 0
	s_nop 0
	s_nop 0
	s_nop 0
	s_nop 0
	s_nop 0
	s_nop 0
	s_nop 0
	s_nop 0
	s_nop 0
	s_nop 0
	s_nop 0
	s_nop 0
	s_nop 0
	s_nop 0
	s_nop 0
	s_nop 0
	s_nop 0
	s_nop 0
	s_nop 0
	s_nop 0
	s_nop 0
	s_nop 0
	s_nop 0
	s_nop 0
	s_nop 0
	s_nop 0
	s_nop 0
	s_nop 0
	s_nop 0
	s_nop 0
	s_nop 0
	s_nop 0
	s_nop 0
	s_nop 0
	s_nop 0
	s_nop 0
	s_nop 0
	s_nop 0
	s_nop 0
	s_nop 0
	s_nop 0
	s_nop 0
	s_nop 0
	s_nop 0
	s_nop 0
	s_nop 0
	s_nop 0
	s_nop 0
	s_nop 0
	s_nop 0
	s_nop 0
	s_nop 0
	s_nop 0
	s_nop 0
	s_nop 0
	s_nop 0
	s_nop 0
	s_nop 0
	s_nop 0
	s_nop 0
	s_nop 0
	s_nop 0
	s_nop 0
	s_nop 0
	s_nop 0
	s_nop 0
	s_nop 0
	s_nop 0
	s_nop 0
	s_nop 0
	s_nop 0
